# P0 int8 weight quantisation: clamp in f32 (v_med3) + round-to-nearest via 1.5*2^23 add instead of rndne/cvt/min/max (same int8 bytes)
# speedup vs baseline: 1.0017x; 1.0017x over previous
.LBB0_127:
	s_or_b64 exec, exec, s[14:15]
	s_mov_b32 s29, 0x42fe0000
	v_mov_b32_e32 v222, 0xc2fe0000
	s_waitcnt lgkmcnt(0)
	s_barrier
	ds_write2_b32 v207, v124, v125 offset1:1
	ds_write2_b32 v207, v126, v127 offset0:2 offset1:3
	v_add_u32_e32 v124, 0x410, v207
	ds_write2_b32 v124, v108, v109 offset1:1
	v_add_u32_e32 v108, 0x418, v207
	ds_write2_b32 v108, v110, v111 offset1:1
	v_add_u32_e32 v111, 0xc30, v207
	ds_write2_b32 v111, v100, v101 offset1:1
	v_add_u32_e32 v100, 0xc38, v207
	ds_write2_b32 v100, v102, v103 offset1:1
	v_add_u32_e32 v103, 0x1450, v207
	ds_write2_b32 v103, v92, v93 offset1:1
	v_add_u32_e32 v92, 0x1458, v207
	ds_write2_b32 v92, v94, v95 offset1:1
	v_add_u32_e32 v95, 0x1c70, v207
	ds_write2_b32 v95, v88, v89 offset1:1
	v_add_u32_e32 v88, 0x1c78, v207
	ds_write2_b32 v88, v90, v91 offset1:1
	v_add_u32_e32 v91, 0x2490, v207
	ds_write2_b32 v91, v84, v85 offset1:1
	v_add_u32_e32 v84, 0x2498, v207
	ds_write2_b32 v84, v86, v87 offset1:1
	v_add_u32_e32 v87, 0x2cb0, v207
	ds_write2_b32 v87, v76, v77 offset1:1
	v_add_u32_e32 v77, 0x2cb8, v207
	v_add_u32_e32 v85, 0x28a0, v207
	ds_write2_b32 v77, v78, v79 offset1:1
	v_add_u32_e32 v78, 0x30c0, v207
	v_add_u32_e32 v79, 0x30c8, v207
	v_add_u32_e32 v109, 0x820, v207
	v_add_u32_e32 v110, 0x828, v207
	v_add_u32_e32 v101, 0x1040, v207
	v_add_u32_e32 v102, 0x1048, v207
	v_add_u32_e32 v93, 0x1860, v207
	v_add_u32_e32 v94, 0x1868, v207
	v_add_u32_e32 v89, 0x2080, v207
	v_add_u32_e32 v90, 0x2088, v207
	ds_write2_b32 v85, v96, v97 offset1:1
	v_add_u32_e32 v86, 0x28a8, v207
	ds_write2_b32 v78, v80, v81 offset1:1
	ds_write2_b32 v79, v82, v83 offset1:1
	v_add_u32_e32 v80, 0x34d0, v207
	v_add_u32_e32 v81, 0x34d8, v207
	v_add_u32_e32 v82, 0x38e0, v207
	v_add_u32_e32 v83, 0x38e8, v207
	v_add_u32_e32 v96, 0x3cf0, v207
	v_add_u32_e32 v97, 0x3cf8, v207
	ds_write2_b32 v109, v120, v121 offset1:1
	ds_write2_b32 v110, v122, v123 offset1:1
	ds_write2_b32 v101, v116, v117 offset1:1
	ds_write2_b32 v102, v118, v119 offset1:1
	ds_write2_b32 v93, v112, v113 offset1:1
	ds_write2_b32 v94, v114, v115 offset1:1
	ds_write2_b32 v89, v104, v105 offset1:1
	ds_write2_b32 v90, v106, v107 offset1:1
	ds_write2_b32 v86, v98, v99 offset1:1
	ds_write2_b32 v80, v68, v69 offset1:1
	ds_write2_b32 v81, v70, v71 offset1:1
	ds_write2_b32 v82, v72, v73 offset1:1
	ds_write2_b32 v83, v74, v75 offset1:1
	ds_write2_b32 v96, v64, v65 offset1:1
	ds_write2_b32 v97, v66, v67 offset1:1
	s_waitcnt lgkmcnt(0)
	ds_read_b32 v98, v202
	ds_read2_b32 v[64:65], v201 offset1:65
	ds_read2_b32 v[66:67], v201 offset0:130 offset1:195
	s_lshl_b64 s[8:9], s[8:9], 21
	v_lshl_add_u64 v[70:71], v[196:197], 0, s[8:9]
	s_movk_i32 s8, 0x7f
	s_waitcnt lgkmcnt(1)
	v_mul_f32_e32 v64, v98, v64
	v_mul_f32_e32 v65, v98, v65
	v_med3_f32 v64, v64, s29, v222
	v_add_f32_e32 v64, 0x4b400000, v64
	v_med3_f32 v65, v65, s29, v222
	v_add_f32_e32 v65, 0x4b400000, v65
	s_movk_i32 s9, 0xff81
	s_waitcnt lgkmcnt(0)
	v_mul_f32_e32 v66, v98, v66
	v_mul_f32_e32 v67, v98, v67
	v_mov_b32_e32 v72, v64
	v_mov_b32_e32 v64, v65
	v_med3_f32 v65, v66, s29, v222
	v_add_f32_e32 v65, 0x4b400000, v65
	v_med3_f32 v66, v67, s29, v222
	v_add_f32_e32 v66, 0x4b400000, v66
	v_lshlrev_b32_e32 v67, 16, v65
	v_mov_b32_e32 v65, v66
	v_lshlrev_b32_e32 v64, 8, v64
	v_add_u32_e32 v74, 0x400, v201
	v_mov_b32_e32 v66, v65
	v_and_b32_e32 v73, 0xff00, v64
	ds_read2_b32 v[64:65], v74 offset0:4 offset1:69
	ds_read2_b32 v[68:69], v74 offset0:134 offset1:199
	v_and_b32_e32 v67, 0xff0000, v67
	v_perm_b32 v66, v66, v72, s24
	s_movk_i32 s8, 0x7f
	s_waitcnt lgkmcnt(1)
	v_mul_f32_e32 v64, v98, v64
	v_mul_f32_e32 v65, v98, v65
	v_med3_f32 v64, v64, s29, v222
	v_add_f32_e32 v64, 0x4b400000, v64
	v_med3_f32 v65, v65, s29, v222
	v_add_f32_e32 v65, 0x4b400000, v65
	s_movk_i32 s9, 0xff81
	v_or3_b32 v66, v66, v73, v67
	s_waitcnt lgkmcnt(0)
	v_mul_f32_e32 v67, v98, v68
	v_mul_f32_e32 v68, v98, v69
	v_mov_b32_e32 v72, v64
	v_mov_b32_e32 v64, v65
	v_med3_f32 v65, v67, s29, v222
	v_add_f32_e32 v65, 0x4b400000, v65
	v_med3_f32 v67, v68, s29, v222
	v_add_f32_e32 v67, 0x4b400000, v67
	v_lshlrev_b32_e32 v68, 16, v65
	v_mov_b32_e32 v65, v67
	v_lshlrev_b32_e32 v64, 8, v64
	v_add_u32_e32 v75, 0x800, v201
	v_mov_b32_e32 v67, v65
	v_and_b32_e32 v73, 0xff00, v64
	ds_read2_b32 v[64:65], v75 offset0:8 offset1:73
	v_and_b32_e32 v76, 0xff0000, v68
	ds_read2_b32 v[68:69], v75 offset0:138 offset1:203
	s_movk_i32 s8, 0x7f
	s_movk_i32 s9, 0xff81
	s_waitcnt lgkmcnt(1)
	v_mul_f32_e32 v64, v98, v64
	v_mul_f32_e32 v65, v98, v65
	v_med3_f32 v64, v64, s29, v222
	v_add_f32_e32 v64, 0x4b400000, v64
	v_med3_f32 v65, v65, s29, v222
	v_add_f32_e32 v65, 0x4b400000, v65
	s_waitcnt lgkmcnt(0)
	v_mul_f32_e32 v68, v98, v68
	v_mul_f32_e32 v69, v98, v69
	v_mov_b32_e32 v99, v64
	v_mov_b32_e32 v64, v65
	v_med3_f32 v65, v68, s29, v222
	v_add_f32_e32 v65, 0x4b400000, v65
	v_med3_f32 v68, v69, s29, v222
	v_add_f32_e32 v68, 0x4b400000, v68
	v_perm_b32 v67, v67, v72, s24
	v_or3_b32 v67, v67, v73, v76
	v_lshlrev_b32_e32 v69, 16, v65
	v_mov_b32_e32 v65, v68
	v_lshlrev_b32_e32 v64, 8, v64
	v_add_u32_e32 v76, 0xc00, v201
	v_mov_b32_e32 v68, v65
	v_and_b32_e32 v104, 0xff00, v64
	ds_read2_b32 v[64:65], v76 offset0:12 offset1:77
	ds_read2_b32 v[72:73], v76 offset0:142 offset1:207
	v_and_b32_e32 v69, 0xff0000, v69
	v_perm_b32 v68, v68, v99, s24
	v_or3_b32 v68, v68, v104, v69
	s_waitcnt lgkmcnt(1)
	v_mul_f32_e32 v64, v98, v64
	v_mul_f32_e32 v65, v98, v65
	s_waitcnt lgkmcnt(0)
	v_mul_f32_e32 v69, v98, v72
	v_mul_f32_e32 v72, v98, v73
	v_med3_f32 v64, v64, s29, v222
	v_med3_f32 v65, v65, s29, v222
	v_med3_f32 v72, v72, s29, v222
	v_add_f32_e32 v64, 0x4b400000, v64
	v_add_f32_e32 v65, 0x4b400000, v65
	v_med3_f32 v69, v69, s29, v222
	v_add_f32_e32 v72, 0x4b400000, v72
	v_add_f32_e32 v69, 0x4b400000, v69
	s_movk_i32 s8, 0x7f
	s_movk_i32 s9, 0xff81
	s_add_i32 s26, s26, s22
	ds_read_b32 v107, v203
	ds_read2_b32 v[98:99], v201 offset0:16 offset1:81
	v_lshlrev_b32_e32 v69, 16, v69
	v_lshlrev_b32_e32 v65, 8, v65
	v_perm_b32 v64, v72, v64, s24
	v_add_u32_e32 v72, s26, v200
	v_and_b32_e32 v65, 0xff00, v65
	v_and_b32_e32 v69, 0xff0000, v69
	v_ashrrev_i32_e32 v73, 31, v72
	v_or3_b32 v69, v64, v65, v69
	v_lshlrev_b64 v[64:65], 10, v[72:73]
	v_lshl_add_u64 v[64:65], v[70:71], 0, v[64:65]
	global_store_dwordx4 v[64:65], v[66:69], off
	ds_read2_b32 v[104:105], v201 offset0:146 offset1:211
	s_movk_i32 s8, 0x7f
	s_waitcnt lgkmcnt(1)
	v_mul_f32_e32 v66, v107, v98
	v_mul_f32_e32 v67, v107, v99
	v_med3_f32 v66, v66, s29, v222
	v_add_f32_e32 v66, 0x4b400000, v66
	v_med3_f32 v67, v67, s29, v222
	v_add_f32_e32 v67, 0x4b400000, v67
	s_movk_i32 s9, 0xff81
	s_waitcnt lgkmcnt(0)
	v_mul_f32_e32 v68, v107, v104
	v_mul_f32_e32 v69, v107, v105
	v_mov_b32_e32 v73, v66
	v_mov_b32_e32 v66, v67
	v_med3_f32 v67, v68, s29, v222
	v_add_f32_e32 v67, 0x4b400000, v67
	v_med3_f32 v68, v69, s29, v222
	v_add_f32_e32 v68, 0x4b400000, v68
	v_lshlrev_b32_e32 v69, 16, v67
	v_mov_b32_e32 v67, v68
	v_lshlrev_b32_e32 v66, 8, v66
	v_mov_b32_e32 v98, v67
	v_and_b32_e32 v99, 0xff00, v66
	ds_read2_b32 v[66:67], v74 offset0:20 offset1:85
	v_and_b32_e32 v104, 0xff0000, v69
	ds_read2_b32 v[68:69], v74 offset0:150 offset1:215
	s_movk_i32 s8, 0x7f
	s_movk_i32 s9, 0xff81
	s_waitcnt lgkmcnt(1)
	v_mul_f32_e32 v66, v107, v66
	v_mul_f32_e32 v67, v107, v67
	v_med3_f32 v66, v66, s29, v222
	v_add_f32_e32 v66, 0x4b400000, v66
	v_med3_f32 v67, v67, s29, v222
	v_add_f32_e32 v67, 0x4b400000, v67
	v_perm_b32 v73, v98, v73, s24
	s_waitcnt lgkmcnt(0)
	v_mul_f32_e32 v68, v107, v68
	v_or3_b32 v104, v73, v99, v104
	v_mul_f32_e32 v69, v107, v69
	v_mov_b32_e32 v73, v66
	v_mov_b32_e32 v66, v67
	v_med3_f32 v67, v68, s29, v222
	v_add_f32_e32 v67, 0x4b400000, v67
	v_med3_f32 v68, v69, s29, v222
	v_add_f32_e32 v68, 0x4b400000, v68
	v_lshlrev_b32_e32 v69, 16, v67
	v_mov_b32_e32 v67, v68
	v_lshlrev_b32_e32 v66, 8, v66
	v_mov_b32_e32 v98, v67
	v_and_b32_e32 v99, 0xff00, v66
	ds_read2_b32 v[66:67], v75 offset0:24 offset1:89
	v_and_b32_e32 v105, 0xff0000, v69
	ds_read2_b32 v[68:69], v75 offset0:154 offset1:219
	s_movk_i32 s8, 0x7f
	s_movk_i32 s9, 0xff81
	s_waitcnt lgkmcnt(1)
	v_mul_f32_e32 v66, v107, v66
	v_mul_f32_e32 v67, v107, v67
	v_med3_f32 v66, v66, s29, v222
	v_add_f32_e32 v66, 0x4b400000, v66
	v_med3_f32 v67, v67, s29, v222
	v_add_f32_e32 v67, 0x4b400000, v67
	v_perm_b32 v73, v98, v73, s24
	s_waitcnt lgkmcnt(0)
	v_mul_f32_e32 v68, v107, v68
	v_or3_b32 v105, v73, v99, v105
	v_mul_f32_e32 v69, v107, v69
	v_mov_b32_e32 v73, v66
	v_mov_b32_e32 v66, v67
	v_med3_f32 v67, v68, s29, v222
	v_add_f32_e32 v67, 0x4b400000, v67
	v_med3_f32 v68, v69, s29, v222
	v_add_f32_e32 v68, 0x4b400000, v68
	v_lshlrev_b32_e32 v69, 16, v67
	v_mov_b32_e32 v67, v68
	v_lshlrev_b32_e32 v66, 8, v66
	v_mov_b32_e32 v98, v67
	v_and_b32_e32 v99, 0xff00, v66
	ds_read2_b32 v[66:67], v76 offset0:28 offset1:93
	v_and_b32_e32 v106, 0xff0000, v69
	ds_read2_b32 v[68:69], v76 offset0:158 offset1:223
	s_movk_i32 s8, 0x7f
	s_movk_i32 s9, 0xff81
	s_waitcnt lgkmcnt(1)
	v_mul_f32_e32 v67, v107, v67
	v_mul_f32_e32 v66, v107, v66
	s_waitcnt lgkmcnt(0)
	v_mul_f32_e32 v68, v107, v68
	v_mul_f32_e32 v69, v107, v69
	v_med3_f32 v67, v67, s29, v222
	v_med3_f32 v66, v66, s29, v222
	v_add_f32_e32 v67, 0x4b400000, v67
	v_med3_f32 v68, v68, s29, v222
	v_med3_f32 v69, v69, s29, v222
	v_add_f32_e32 v66, 0x4b400000, v66
	v_add_f32_e32 v68, 0x4b400000, v68
	v_add_f32_e32 v69, 0x4b400000, v69
	v_perm_b32 v73, v98, v73, s24
	v_lshlrev_b32_e32 v68, 16, v68
	v_lshlrev_b32_e32 v67, 8, v67
	v_and_b32_e32 v67, 0xff00, v67
	v_and_b32_e32 v68, 0xff0000, v68
	v_perm_b32 v66, v69, v66, s24
	v_or3_b32 v106, v73, v99, v106
	v_or3_b32 v107, v66, v67, v68
	ds_read_b32 v73, v204
	ds_read2_b32 v[68:69], v201 offset0:32 offset1:97
	ds_read2_b32 v[98:99], v201 offset0:162 offset1:227
	v_add_u32_e32 v66, 16, v72
	v_ashrrev_i32_e32 v67, 31, v66
	v_lshlrev_b64 v[66:67], 10, v[66:67]
	s_waitcnt lgkmcnt(1)
	v_mul_f32_e32 v68, v73, v68
	v_mul_f32_e32 v69, v73, v69
	v_med3_f32 v68, v68, s29, v222
	v_add_f32_e32 v68, 0x4b400000, v68
	v_med3_f32 v69, v69, s29, v222
	v_add_f32_e32 v69, 0x4b400000, v69
	v_lshl_add_u64 v[66:67], v[70:71], 0, v[66:67]
	s_movk_i32 s8, 0x7f
	s_movk_i32 s9, 0xff81
	global_store_dwordx4 v[66:67], v[104:107], off
	s_waitcnt lgkmcnt(0)
	v_mul_f32_e32 v98, v73, v98
	v_mul_f32_e32 v99, v73, v99
	v_mov_b32_e32 v104, v68
	v_mov_b32_e32 v68, v69
	v_med3_f32 v69, v98, s29, v222
	v_add_f32_e32 v69, 0x4b400000, v69
	v_med3_f32 v98, v99, s29, v222
	v_add_f32_e32 v98, 0x4b400000, v98
	v_lshlrev_b32_e32 v99, 16, v69
	v_mov_b32_e32 v69, v98
	v_lshlrev_b32_e32 v68, 8, v68
	v_mov_b32_e32 v105, v69
	v_and_b32_e32 v106, 0xff00, v68
	ds_read2_b32 v[68:69], v74 offset0:36 offset1:101
	v_and_b32_e32 v107, 0xff0000, v99
	ds_read2_b32 v[98:99], v74 offset0:166 offset1:231
	s_movk_i32 s8, 0x7f
	s_movk_i32 s9, 0xff81
	s_waitcnt lgkmcnt(1)
	v_mul_f32_e32 v68, v73, v68
	v_mul_f32_e32 v69, v73, v69
	v_med3_f32 v68, v68, s29, v222
	v_add_f32_e32 v68, 0x4b400000, v68
	v_med3_f32 v69, v69, s29, v222
	v_add_f32_e32 v69, 0x4b400000, v69
	s_waitcnt lgkmcnt(0)
	v_mul_f32_e32 v98, v73, v98
	v_perm_b32 v104, v105, v104, s24
	v_mul_f32_e32 v99, v73, v99
	v_mov_b32_e32 v105, v68
	v_mov_b32_e32 v68, v69
	v_med3_f32 v69, v98, s29, v222
	v_add_f32_e32 v69, 0x4b400000, v69
	v_med3_f32 v98, v99, s29, v222
	v_add_f32_e32 v98, 0x4b400000, v98
	v_lshlrev_b32_e32 v99, 16, v69
	v_mov_b32_e32 v69, v98
	v_lshlrev_b32_e32 v68, 8, v68
	v_or3_b32 v104, v104, v106, v107
	v_mov_b32_e32 v106, v69
	v_and_b32_e32 v107, 0xff00, v68
	ds_read2_b32 v[68:69], v75 offset0:40 offset1:105
	v_and_b32_e32 v112, 0xff0000, v99
	ds_read2_b32 v[98:99], v75 offset0:170 offset1:235
	s_movk_i32 s8, 0x7f
	s_movk_i32 s9, 0xff81
	s_waitcnt lgkmcnt(1)
	v_mul_f32_e32 v68, v73, v68
	v_mul_f32_e32 v69, v73, v69
	v_med3_f32 v68, v68, s29, v222
	v_add_f32_e32 v68, 0x4b400000, v68
	v_med3_f32 v69, v69, s29, v222
	v_add_f32_e32 v69, 0x4b400000, v69
	s_waitcnt lgkmcnt(0)
	v_mul_f32_e32 v98, v73, v98
	v_perm_b32 v105, v106, v105, s24
	v_mul_f32_e32 v99, v73, v99
	v_mov_b32_e32 v106, v68
	v_mov_b32_e32 v68, v69
	v_med3_f32 v69, v98, s29, v222
	v_add_f32_e32 v69, 0x4b400000, v69
	v_med3_f32 v98, v99, s29, v222
	v_add_f32_e32 v98, 0x4b400000, v98
	v_lshlrev_b32_e32 v99, 16, v69
	v_mov_b32_e32 v69, v98
	v_lshlrev_b32_e32 v68, 8, v68
	v_or3_b32 v105, v105, v107, v112
	v_mov_b32_e32 v107, v69
	v_and_b32_e32 v112, 0xff00, v68
	ds_read2_b32 v[68:69], v76 offset0:44 offset1:109
	v_and_b32_e32 v113, 0xff0000, v99
	ds_read2_b32 v[98:99], v76 offset0:174 offset1:239
	s_movk_i32 s8, 0x7f
	s_movk_i32 s9, 0xff81
	s_waitcnt lgkmcnt(1)
	v_mul_f32_e32 v69, v73, v69
	v_mul_f32_e32 v68, v73, v68
	s_waitcnt lgkmcnt(0)
	v_mul_f32_e32 v98, v73, v98
	v_mul_f32_e32 v73, v73, v99
	v_med3_f32 v69, v69, s29, v222
	v_med3_f32 v68, v68, s29, v222
	v_add_f32_e32 v69, 0x4b400000, v69
	v_med3_f32 v98, v98, s29, v222
	v_med3_f32 v73, v73, s29, v222
	v_add_f32_e32 v68, 0x4b400000, v68
	v_add_f32_e32 v98, 0x4b400000, v98
	v_add_f32_e32 v73, 0x4b400000, v73
	v_perm_b32 v106, v107, v106, s24
	v_lshlrev_b32_e32 v98, 16, v98
	v_lshlrev_b32_e32 v69, 8, v69
	v_and_b32_e32 v69, 0xff00, v69
	v_and_b32_e32 v98, 0xff0000, v98
	v_perm_b32 v68, v73, v68, s24
	v_or3_b32 v107, v68, v69, v98
	ds_read_b32 v73, v205
	ds_read2_b32 v[98:99], v201 offset0:48 offset1:113
	v_or3_b32 v106, v106, v112, v113
	ds_read2_b32 v[112:113], v201 offset0:178 offset1:243
	v_add_u32_e32 v68, 32, v72
	v_ashrrev_i32_e32 v69, 31, v68
	s_waitcnt lgkmcnt(1)
	v_mul_f32_e32 v98, v73, v98
	v_mul_f32_e32 v99, v73, v99
	v_med3_f32 v98, v98, s29, v222
	v_add_f32_e32 v98, 0x4b400000, v98
	v_med3_f32 v99, v99, s29, v222
	v_add_f32_e32 v99, 0x4b400000, v99
	v_lshlrev_b64 v[68:69], 10, v[68:69]
	v_lshl_add_u64 v[68:69], v[70:71], 0, v[68:69]
	s_movk_i32 s8, 0x7f
	s_movk_i32 s9, 0xff81
	global_store_dwordx4 v[68:69], v[104:107], off
	ds_read2_b32 v[106:107], v74 offset0:182 offset1:247
	s_waitcnt lgkmcnt(1)
	v_mul_f32_e32 v104, v73, v112
	v_mul_f32_e32 v105, v73, v113
	v_mov_b32_e32 v112, v98
	v_mov_b32_e32 v98, v99
	v_med3_f32 v99, v104, s29, v222
	v_add_f32_e32 v99, 0x4b400000, v99
	v_med3_f32 v104, v105, s29, v222
	v_add_f32_e32 v104, 0x4b400000, v104
	v_lshlrev_b32_e32 v105, 16, v99
	v_mov_b32_e32 v99, v104
	v_lshlrev_b32_e32 v98, 8, v98
	v_mov_b32_e32 v104, v99
	v_and_b32_e32 v113, 0xff00, v98
	ds_read2_b32 v[98:99], v74 offset0:52 offset1:117
	v_and_b32_e32 v105, 0xff0000, v105
	v_perm_b32 v104, v104, v112, s24
	s_movk_i32 s8, 0x7f
	s_movk_i32 s9, 0xff81
	s_waitcnt lgkmcnt(0)
	v_mul_f32_e32 v98, v73, v98
	v_mul_f32_e32 v99, v73, v99
	v_med3_f32 v98, v98, s29, v222
	v_add_f32_e32 v98, 0x4b400000, v98
	v_med3_f32 v99, v99, s29, v222
	v_add_f32_e32 v99, 0x4b400000, v99
	v_or3_b32 v104, v104, v113, v105
	v_mul_f32_e32 v105, v73, v106
	v_mul_f32_e32 v106, v73, v107
	v_mov_b32_e32 v112, v98
	v_mov_b32_e32 v98, v99
	v_med3_f32 v99, v105, s29, v222
	v_add_f32_e32 v99, 0x4b400000, v99
	v_med3_f32 v105, v106, s29, v222
	v_add_f32_e32 v105, 0x4b400000, v105
	v_lshlrev_b32_e32 v106, 16, v99
	v_mov_b32_e32 v99, v105
	v_lshlrev_b32_e32 v98, 8, v98
	v_mov_b32_e32 v105, v99
	v_and_b32_e32 v113, 0xff00, v98
	ds_read2_b32 v[98:99], v75 offset0:56 offset1:121
	v_and_b32_e32 v114, 0xff0000, v106
	ds_read2_b32 v[106:107], v75 offset0:186 offset1:251
	s_movk_i32 s8, 0x7f
	s_movk_i32 s9, 0xff81
	s_waitcnt lgkmcnt(1)
	v_mul_f32_e32 v98, v73, v98
	v_mul_f32_e32 v99, v73, v99
	v_med3_f32 v98, v98, s29, v222
	v_add_f32_e32 v98, 0x4b400000, v98
	v_med3_f32 v99, v99, s29, v222
	v_add_f32_e32 v99, 0x4b400000, v99
	v_perm_b32 v105, v105, v112, s24
	s_waitcnt lgkmcnt(0)
	v_mul_f32_e32 v106, v73, v106
	v_or3_b32 v105, v105, v113, v114
	v_mul_f32_e32 v107, v73, v107
	v_mov_b32_e32 v114, v98
	v_mov_b32_e32 v98, v99
	v_med3_f32 v99, v106, s29, v222
	v_add_f32_e32 v99, 0x4b400000, v99
	v_med3_f32 v106, v107, s29, v222
	v_add_f32_e32 v106, 0x4b400000, v106
	v_lshlrev_b32_e32 v107, 16, v99
	v_mov_b32_e32 v99, v106
	v_lshlrev_b32_e32 v98, 8, v98
	v_mov_b32_e32 v106, v99
	v_and_b32_e32 v115, 0xff00, v98
	ds_read2_b32 v[98:99], v76 offset0:60 offset1:125
	ds_read2_b32 v[112:113], v76 offset0:190 offset1:255
	v_and_b32_e32 v107, 0xff0000, v107
	v_perm_b32 v106, v106, v114, s24
	v_or3_b32 v106, v106, v115, v107
	s_waitcnt lgkmcnt(1)
	v_mul_f32_e32 v99, v73, v99
	v_mul_f32_e32 v98, v73, v98
	s_waitcnt lgkmcnt(0)
	v_mul_f32_e32 v107, v73, v112
	v_mul_f32_e32 v73, v73, v113
	v_med3_f32 v99, v99, s29, v222
	v_med3_f32 v98, v98, s29, v222
	v_add_f32_e32 v99, 0x4b400000, v99
	v_med3_f32 v107, v107, s29, v222
	v_med3_f32 v73, v73, s29, v222
	v_add_f32_e32 v98, 0x4b400000, v98
	v_add_f32_e32 v107, 0x4b400000, v107
	v_add_f32_e32 v73, 0x4b400000, v73
	s_movk_i32 s8, 0x7f
	s_movk_i32 s9, 0xff81
	v_add_u32_e32 v72, 48, v72
	v_lshlrev_b32_e32 v107, 16, v107
	v_lshlrev_b32_e32 v99, 8, v99
	v_and_b32_e32 v99, 0xff00, v99
	v_and_b32_e32 v107, 0xff0000, v107
	v_perm_b32 v73, v73, v98, s24
	v_or3_b32 v107, v73, v99, v107
	v_ashrrev_i32_e32 v73, 31, v72
	v_lshlrev_b64 v[72:73], 10, v[72:73]
	v_lshl_add_u64 v[70:71], v[70:71], 0, v[72:73]
	global_store_dwordx4 v[70:71], v[104:107], off
	s_waitcnt lgkmcnt(0)
	ds_write2_b32 v207, v4, v5 offset1:1
	ds_write2_b32 v207, v6, v7 offset0:2 offset1:3
	ds_write2_b32 v124, v0, v1 offset1:1
	ds_write2_b32 v108, v2, v3 offset1:1
	ds_write2_b32 v109, v12, v13 offset1:1
	ds_write2_b32 v110, v14, v15 offset1:1
	ds_write2_b32 v111, v8, v9 offset1:1
	ds_write2_b32 v100, v10, v11 offset1:1
	ds_write2_b32 v101, v20, v21 offset1:1
	ds_write2_b32 v102, v22, v23 offset1:1
	ds_write2_b32 v103, v16, v17 offset1:1
	ds_write2_b32 v92, v18, v19 offset1:1
	ds_write2_b32 v93, v28, v29 offset1:1
	ds_write2_b32 v94, v30, v31 offset1:1
	ds_write2_b32 v95, v24, v25 offset1:1
	ds_write2_b32 v88, v26, v27 offset1:1
	ds_write2_b32 v89, v36, v37 offset1:1
	ds_write2_b32 v90, v38, v39 offset1:1
	ds_write2_b32 v91, v32, v33 offset1:1
	ds_write2_b32 v84, v34, v35 offset1:1
	ds_write2_b32 v85, v44, v45 offset1:1
	ds_write2_b32 v86, v46, v47 offset1:1
	ds_write2_b32 v87, v40, v41 offset1:1
	ds_write2_b32 v77, v42, v43 offset1:1
	ds_write2_b32 v78, v52, v53 offset1:1
	ds_write2_b32 v79, v54, v55 offset1:1
	ds_write2_b32 v80, v48, v49 offset1:1
	ds_write2_b32 v81, v50, v51 offset1:1
	ds_write2_b32 v82, v60, v61 offset1:1
	ds_write2_b32 v83, v62, v63 offset1:1
	ds_write2_b32 v96, v56, v57 offset1:1
	ds_write2_b32 v97, v58, v59 offset1:1
	s_waitcnt lgkmcnt(0)
	ds_read_b32 v8, v202
	ds_read2_b32 v[0:1], v201 offset1:65
	ds_read2_b32 v[2:3], v201 offset0:130 offset1:195
	s_movk_i32 s8, 0x7f
	s_movk_i32 s9, 0xff81
	s_waitcnt lgkmcnt(1)
	v_mul_f32_e32 v1, v8, v1
	s_waitcnt lgkmcnt(0)
	v_mul_f32_e32 v2, v8, v2
	v_mul_f32_e32 v3, v8, v3
	v_med3_f32 v2, v2, s29, v222
	v_add_f32_e32 v2, 0x4b400000, v2
	v_med3_f32 v3, v3, s29, v222
	v_add_f32_e32 v3, 0x4b400000, v3
	v_mul_f32_e32 v0, v8, v0
	v_med3_f32 v1, v1, s29, v222
	v_med3_f32 v0, v0, s29, v222
	v_add_f32_e32 v1, 0x4b400000, v1
	v_add_f32_e32 v0, 0x4b400000, v0
	v_lshlrev_b32_e32 v4, 16, v2
	v_mov_b32_e32 v2, v3
	v_mov_b32_e32 v6, v2
	ds_read2_b32 v[2:3], v74 offset0:4 offset1:69
	v_and_b32_e32 v7, 0xff0000, v4
	ds_read2_b32 v[4:5], v74 offset0:134 offset1:199
	v_lshlrev_b32_e32 v1, 8, v1
	v_and_b32_e32 v1, 0xff00, v1
	v_perm_b32 v0, v6, v0, s24
	v_or3_b32 v0, v0, v1, v7
	s_waitcnt lgkmcnt(1)
	v_mul_f32_e32 v1, v8, v2
	v_mul_f32_e32 v2, v8, v3
	s_waitcnt lgkmcnt(0)
	v_mul_f32_e32 v3, v8, v4
	v_med3_f32 v3, v3, s29, v222
	v_mul_f32_e32 v4, v8, v5
	v_add_f32_e32 v3, 0x4b400000, v3
	v_med3_f32 v2, v2, s29, v222
	v_med3_f32 v4, v4, s29, v222
	v_add_f32_e32 v2, 0x4b400000, v2
	v_add_f32_e32 v4, 0x4b400000, v4
	s_movk_i32 s8, 0x7f
	s_movk_i32 s9, 0xff81
	v_med3_f32 v1, v1, s29, v222
	v_lshlrev_b32_e32 v5, 16, v3
	v_mov_b32_e32 v3, v4
	v_and_b32_e32 v9, 0xff0000, v5
	ds_read2_b32 v[4:5], v75 offset0:138 offset1:203
	v_lshlrev_b32_e32 v2, 8, v2
	v_mov_b32_e32 v6, v3
	v_and_b32_e32 v7, 0xff00, v2
	ds_read2_b32 v[2:3], v75 offset0:8 offset1:73
	v_add_f32_e32 v1, 0x4b400000, v1
	s_waitcnt lgkmcnt(1)
	v_mul_f32_e32 v4, v8, v4
	v_mul_f32_e32 v5, v8, v5
	v_med3_f32 v4, v4, s29, v222
	v_add_f32_e32 v4, 0x4b400000, v4
	v_med3_f32 v5, v5, s29, v222
	s_waitcnt lgkmcnt(0)
	v_mul_f32_e32 v3, v8, v3
	v_add_f32_e32 v5, 0x4b400000, v5
	v_mul_f32_e32 v2, v8, v2
	v_med3_f32 v3, v3, s29, v222
	s_movk_i32 s8, 0x7f
	s_movk_i32 s9, 0xff81
	v_med3_f32 v2, v2, s29, v222
	v_add_f32_e32 v3, 0x4b400000, v3
	v_add_f32_e32 v2, 0x4b400000, v2
	v_perm_b32 v1, v6, v1, s24
	v_lshlrev_b32_e32 v6, 16, v4
	v_mov_b32_e32 v4, v5
	v_or3_b32 v1, v1, v7, v9
	v_mov_b32_e32 v9, v4
	ds_read2_b32 v[4:5], v76 offset0:12 offset1:77
	v_and_b32_e32 v10, 0xff0000, v6
	ds_read2_b32 v[6:7], v76 offset0:142 offset1:207
	v_lshlrev_b32_e32 v3, 8, v3
	v_and_b32_e32 v3, 0xff00, v3
	v_perm_b32 v2, v9, v2, s24
	v_or3_b32 v2, v2, v3, v10
	s_waitcnt lgkmcnt(1)
	v_mul_f32_e32 v3, v8, v4
	v_mul_f32_e32 v4, v8, v5
	s_waitcnt lgkmcnt(0)
	v_mul_f32_e32 v5, v8, v6
	v_mul_f32_e32 v6, v8, v7
	v_med3_f32 v4, v4, s29, v222
	v_med3_f32 v3, v3, s29, v222
	v_add_f32_e32 v4, 0x4b400000, v4
	v_med3_f32 v5, v5, s29, v222
	v_med3_f32 v6, v6, s29, v222
	v_add_f32_e32 v3, 0x4b400000, v3
	v_add_f32_e32 v5, 0x4b400000, v5
	v_add_f32_e32 v6, 0x4b400000, v6
	s_movk_i32 s8, 0x7f
	s_movk_i32 s9, 0xff81
	s_add_i32 s25, s25, s53
	v_lshlrev_b32_e32 v5, 16, v5
	v_lshlrev_b32_e32 v4, 8, v4
	v_and_b32_e32 v8, 0xff00, v4
	v_and_b32_e32 v9, 0xff0000, v5
	ds_read_b32 v10, v203
	ds_read2_b32 v[4:5], v201 offset0:16 offset1:81
	v_perm_b32 v3, v6, v3, s24
	ds_read2_b32 v[6:7], v201 offset0:146 offset1:211
	v_or3_b32 v3, v3, v8, v9
	global_store_dwordx4 v[64:65], v[0:3], off offset:64
	s_movk_i32 s8, 0x7f
	s_movk_i32 s9, 0xff81
	s_waitcnt lgkmcnt(0)
	v_mul_f32_e32 v2, v10, v6
	v_mul_f32_e32 v3, v10, v7
	v_med3_f32 v2, v2, s29, v222
	v_add_f32_e32 v2, 0x4b400000, v2
	v_med3_f32 v3, v3, s29, v222
	v_mul_f32_e32 v1, v10, v5
	v_add_f32_e32 v3, 0x4b400000, v3
	v_mul_f32_e32 v0, v10, v4
	v_med3_f32 v1, v1, s29, v222
	v_med3_f32 v0, v0, s29, v222
	v_add_f32_e32 v1, 0x4b400000, v1
	v_add_f32_e32 v0, 0x4b400000, v0
	s_add_i32 s22, s22, s23
	v_lshlrev_b32_e32 v4, 16, v2
	v_mov_b32_e32 v2, v3
	v_mov_b32_e32 v6, v2
	ds_read2_b32 v[2:3], v74 offset0:20 offset1:85
	v_and_b32_e32 v7, 0xff0000, v4
	ds_read2_b32 v[4:5], v74 offset0:150 offset1:215
	v_lshlrev_b32_e32 v1, 8, v1
	v_and_b32_e32 v1, 0xff00, v1
	v_perm_b32 v0, v6, v0, s24
	v_or3_b32 v0, v0, v1, v7
	s_waitcnt lgkmcnt(1)
	v_mul_f32_e32 v1, v10, v2
	v_mul_f32_e32 v2, v10, v3
	s_waitcnt lgkmcnt(0)
	v_mul_f32_e32 v3, v10, v4
	v_med3_f32 v3, v3, s29, v222
	v_mul_f32_e32 v4, v10, v5
	v_add_f32_e32 v3, 0x4b400000, v3
	v_med3_f32 v2, v2, s29, v222
	v_med3_f32 v4, v4, s29, v222
	v_add_f32_e32 v2, 0x4b400000, v2
	v_add_f32_e32 v4, 0x4b400000, v4
	s_movk_i32 s8, 0x7f
	s_movk_i32 s9, 0xff81
	v_med3_f32 v1, v1, s29, v222
	v_lshlrev_b32_e32 v5, 16, v3
	v_mov_b32_e32 v3, v4
	v_and_b32_e32 v8, 0xff0000, v5
	ds_read2_b32 v[4:5], v75 offset0:154 offset1:219
	v_lshlrev_b32_e32 v2, 8, v2
	v_mov_b32_e32 v6, v3
	v_and_b32_e32 v7, 0xff00, v2
	ds_read2_b32 v[2:3], v75 offset0:24 offset1:89
	v_add_f32_e32 v1, 0x4b400000, v1
	s_waitcnt lgkmcnt(1)
	v_mul_f32_e32 v4, v10, v4
	v_mul_f32_e32 v5, v10, v5
	v_med3_f32 v4, v4, s29, v222
	v_add_f32_e32 v4, 0x4b400000, v4
	v_med3_f32 v5, v5, s29, v222
	s_waitcnt lgkmcnt(0)
	v_mul_f32_e32 v3, v10, v3
	v_add_f32_e32 v5, 0x4b400000, v5
	v_mul_f32_e32 v2, v10, v2
	v_med3_f32 v3, v3, s29, v222
	s_movk_i32 s8, 0x7f
	s_movk_i32 s9, 0xff81
	v_med3_f32 v2, v2, s29, v222
	v_add_f32_e32 v3, 0x4b400000, v3
	v_add_f32_e32 v2, 0x4b400000, v2
	v_perm_b32 v1, v6, v1, s24
	v_lshlrev_b32_e32 v6, 16, v4
	v_mov_b32_e32 v4, v5
	v_or3_b32 v1, v1, v7, v8
	v_mov_b32_e32 v8, v4
	ds_read2_b32 v[4:5], v76 offset0:28 offset1:93
	v_and_b32_e32 v9, 0xff0000, v6
	ds_read2_b32 v[6:7], v76 offset0:158 offset1:223
	v_lshlrev_b32_e32 v3, 8, v3
	v_and_b32_e32 v3, 0xff00, v3
	v_perm_b32 v2, v8, v2, s24
	v_or3_b32 v2, v2, v3, v9
	s_waitcnt lgkmcnt(1)
	v_mul_f32_e32 v3, v10, v4
	v_mul_f32_e32 v4, v10, v5
	s_waitcnt lgkmcnt(0)
	v_mul_f32_e32 v5, v10, v6
	v_mul_f32_e32 v6, v10, v7
	v_med3_f32 v4, v4, s29, v222
	v_med3_f32 v3, v3, s29, v222
	v_add_f32_e32 v4, 0x4b400000, v4
	v_med3_f32 v5, v5, s29, v222
	v_med3_f32 v6, v6, s29, v222
	v_add_f32_e32 v3, 0x4b400000, v3
	v_add_f32_e32 v5, 0x4b400000, v5
	v_add_f32_e32 v6, 0x4b400000, v6
	s_movk_i32 s8, 0x7f
	s_movk_i32 s9, 0xff81
	s_cmpk_lt_i32 s25, 0x1000
	v_lshlrev_b32_e32 v5, 16, v5
	v_lshlrev_b32_e32 v4, 8, v4
	v_and_b32_e32 v8, 0xff00, v4
	v_and_b32_e32 v9, 0xff0000, v5
	ds_read_b32 v10, v204
	ds_read2_b32 v[4:5], v201 offset0:32 offset1:97
	v_perm_b32 v3, v6, v3, s24
	ds_read2_b32 v[6:7], v201 offset0:162 offset1:227
	v_or3_b32 v3, v3, v8, v9
	global_store_dwordx4 v[66:67], v[0:3], off offset:64
	s_movk_i32 s8, 0x7f
	s_movk_i32 s9, 0xff81
	s_waitcnt lgkmcnt(0)
	v_mul_f32_e32 v2, v10, v6
	v_mul_f32_e32 v3, v10, v7
	v_med3_f32 v2, v2, s29, v222
	v_add_f32_e32 v2, 0x4b400000, v2
	v_med3_f32 v3, v3, s29, v222
	v_mul_f32_e32 v1, v10, v5
	v_add_f32_e32 v3, 0x4b400000, v3
	v_mul_f32_e32 v0, v10, v4
	v_med3_f32 v1, v1, s29, v222
	v_med3_f32 v0, v0, s29, v222
	v_add_f32_e32 v1, 0x4b400000, v1
	v_add_f32_e32 v0, 0x4b400000, v0
	s_nop 0
	v_lshlrev_b32_e32 v4, 16, v2
	v_mov_b32_e32 v2, v3
	v_mov_b32_e32 v6, v2
	ds_read2_b32 v[2:3], v74 offset0:36 offset1:101
	v_and_b32_e32 v7, 0xff0000, v4
	ds_read2_b32 v[4:5], v74 offset0:166 offset1:231
	v_lshlrev_b32_e32 v1, 8, v1
	v_and_b32_e32 v1, 0xff00, v1
	v_perm_b32 v0, v6, v0, s24
	v_or3_b32 v0, v0, v1, v7
	s_waitcnt lgkmcnt(1)
	v_mul_f32_e32 v1, v10, v2
	v_mul_f32_e32 v2, v10, v3
	s_waitcnt lgkmcnt(0)
	v_mul_f32_e32 v3, v10, v4
	v_med3_f32 v3, v3, s29, v222
	v_mul_f32_e32 v4, v10, v5
	v_add_f32_e32 v3, 0x4b400000, v3
	v_med3_f32 v2, v2, s29, v222
	v_med3_f32 v4, v4, s29, v222
	v_add_f32_e32 v2, 0x4b400000, v2
	v_add_f32_e32 v4, 0x4b400000, v4
	s_movk_i32 s8, 0x7f
	s_movk_i32 s9, 0xff81
	v_med3_f32 v1, v1, s29, v222
	v_lshlrev_b32_e32 v5, 16, v3
	v_mov_b32_e32 v3, v4
	v_and_b32_e32 v8, 0xff0000, v5
	ds_read2_b32 v[4:5], v75 offset0:170 offset1:235
	v_lshlrev_b32_e32 v2, 8, v2
	v_mov_b32_e32 v6, v3
	v_and_b32_e32 v7, 0xff00, v2
	ds_read2_b32 v[2:3], v75 offset0:40 offset1:105
	v_add_f32_e32 v1, 0x4b400000, v1
	s_waitcnt lgkmcnt(1)
	v_mul_f32_e32 v4, v10, v4
	v_mul_f32_e32 v5, v10, v5
	v_med3_f32 v4, v4, s29, v222
	v_add_f32_e32 v4, 0x4b400000, v4
	v_med3_f32 v5, v5, s29, v222
	s_waitcnt lgkmcnt(0)
	v_mul_f32_e32 v3, v10, v3
	v_add_f32_e32 v5, 0x4b400000, v5
	v_mul_f32_e32 v2, v10, v2
	v_med3_f32 v3, v3, s29, v222
	s_movk_i32 s8, 0x7f
	s_movk_i32 s9, 0xff81
	v_med3_f32 v2, v2, s29, v222
	v_add_f32_e32 v3, 0x4b400000, v3
	v_add_f32_e32 v2, 0x4b400000, v2
	v_perm_b32 v1, v6, v1, s24
	v_lshlrev_b32_e32 v6, 16, v4
	v_mov_b32_e32 v4, v5
	v_or3_b32 v1, v1, v7, v8
	v_mov_b32_e32 v8, v4
	ds_read2_b32 v[4:5], v76 offset0:44 offset1:109
	v_and_b32_e32 v9, 0xff0000, v6
	ds_read2_b32 v[6:7], v76 offset0:174 offset1:239
	v_lshlrev_b32_e32 v3, 8, v3
	v_and_b32_e32 v3, 0xff00, v3
	v_perm_b32 v2, v8, v2, s24
	v_or3_b32 v2, v2, v3, v9
	s_waitcnt lgkmcnt(1)
	v_mul_f32_e32 v3, v10, v4
	v_mul_f32_e32 v4, v10, v5
	s_waitcnt lgkmcnt(0)
	v_mul_f32_e32 v5, v10, v6
	v_mul_f32_e32 v6, v10, v7
	v_med3_f32 v4, v4, s29, v222
	v_med3_f32 v3, v3, s29, v222
	v_add_f32_e32 v4, 0x4b400000, v4
	v_med3_f32 v5, v5, s29, v222
	v_med3_f32 v6, v6, s29, v222
	v_add_f32_e32 v3, 0x4b400000, v3
	v_add_f32_e32 v5, 0x4b400000, v5
	v_add_f32_e32 v6, 0x4b400000, v6
	s_movk_i32 s8, 0x7f
	s_movk_i32 s9, 0xff81
	s_nop 0
	v_lshlrev_b32_e32 v5, 16, v5
	v_lshlrev_b32_e32 v4, 8, v4
	v_and_b32_e32 v8, 0xff00, v4
	v_and_b32_e32 v9, 0xff0000, v5
	ds_read_b32 v10, v205
	ds_read2_b32 v[4:5], v201 offset0:48 offset1:113
	v_perm_b32 v3, v6, v3, s24
	ds_read2_b32 v[6:7], v201 offset0:178 offset1:243
	v_or3_b32 v3, v3, v8, v9
	global_store_dwordx4 v[68:69], v[0:3], off offset:64
	s_movk_i32 s8, 0x7f
	s_movk_i32 s9, 0xff81
	s_waitcnt lgkmcnt(0)
	v_mul_f32_e32 v2, v10, v6
	v_mul_f32_e32 v3, v10, v7
	v_med3_f32 v2, v2, s29, v222
	v_add_f32_e32 v2, 0x4b400000, v2
	v_med3_f32 v3, v3, s29, v222
	v_mul_f32_e32 v1, v10, v5
	v_add_f32_e32 v3, 0x4b400000, v3
	v_mul_f32_e32 v0, v10, v4
	v_med3_f32 v1, v1, s29, v222
	v_med3_f32 v0, v0, s29, v222
	v_add_f32_e32 v1, 0x4b400000, v1
	v_add_f32_e32 v0, 0x4b400000, v0
	s_nop 0
	v_lshlrev_b32_e32 v4, 16, v2
	v_mov_b32_e32 v2, v3
	v_mov_b32_e32 v6, v2
	ds_read2_b32 v[2:3], v74 offset0:52 offset1:117
	v_and_b32_e32 v7, 0xff0000, v4
	ds_read2_b32 v[4:5], v74 offset0:182 offset1:247
	v_lshlrev_b32_e32 v1, 8, v1
	v_and_b32_e32 v1, 0xff00, v1
	v_perm_b32 v0, v6, v0, s24
	v_or3_b32 v0, v0, v1, v7
	s_waitcnt lgkmcnt(1)
	v_mul_f32_e32 v1, v10, v2
	v_mul_f32_e32 v2, v10, v3
	s_waitcnt lgkmcnt(0)
	v_mul_f32_e32 v3, v10, v4
	v_med3_f32 v3, v3, s29, v222
	v_mul_f32_e32 v4, v10, v5
	v_add_f32_e32 v3, 0x4b400000, v3
	v_med3_f32 v2, v2, s29, v222
	v_med3_f32 v4, v4, s29, v222
	v_add_f32_e32 v2, 0x4b400000, v2
	v_add_f32_e32 v4, 0x4b400000, v4
	s_movk_i32 s8, 0x7f
	s_movk_i32 s9, 0xff81
	v_med3_f32 v1, v1, s29, v222
	v_lshlrev_b32_e32 v5, 16, v3
	v_mov_b32_e32 v3, v4
	v_and_b32_e32 v8, 0xff0000, v5
	ds_read2_b32 v[4:5], v75 offset0:186 offset1:251
	v_lshlrev_b32_e32 v2, 8, v2
	v_mov_b32_e32 v6, v3
	v_and_b32_e32 v7, 0xff00, v2
	ds_read2_b32 v[2:3], v75 offset0:56 offset1:121
	v_add_f32_e32 v1, 0x4b400000, v1
	s_waitcnt lgkmcnt(1)
	v_mul_f32_e32 v4, v10, v4
	v_mul_f32_e32 v5, v10, v5
	v_med3_f32 v4, v4, s29, v222
	v_add_f32_e32 v4, 0x4b400000, v4
	v_med3_f32 v5, v5, s29, v222
	s_waitcnt lgkmcnt(0)
	v_mul_f32_e32 v3, v10, v3
	v_add_f32_e32 v5, 0x4b400000, v5
	v_mul_f32_e32 v2, v10, v2
	v_med3_f32 v3, v3, s29, v222
	s_movk_i32 s8, 0x7f
	s_movk_i32 s9, 0xff81
	v_med3_f32 v2, v2, s29, v222
	v_add_f32_e32 v3, 0x4b400000, v3
	v_add_f32_e32 v2, 0x4b400000, v2
	v_perm_b32 v1, v6, v1, s24
	v_lshlrev_b32_e32 v6, 16, v4
	v_mov_b32_e32 v4, v5
	v_or3_b32 v1, v1, v7, v8
	v_mov_b32_e32 v8, v4
	ds_read2_b32 v[4:5], v76 offset0:60 offset1:125
	v_and_b32_e32 v9, 0xff0000, v6
	ds_read2_b32 v[6:7], v76 offset0:190 offset1:255
	v_lshlrev_b32_e32 v3, 8, v3
	v_and_b32_e32 v3, 0xff00, v3
	v_perm_b32 v2, v8, v2, s24
	v_or3_b32 v2, v2, v3, v9
	s_waitcnt lgkmcnt(1)
	v_mul_f32_e32 v3, v10, v4
	v_mul_f32_e32 v4, v10, v5
	s_waitcnt lgkmcnt(0)
	v_mul_f32_e32 v5, v10, v6
	v_mul_f32_e32 v6, v10, v7
	v_med3_f32 v4, v4, s29, v222
	v_med3_f32 v3, v3, s29, v222
	v_add_f32_e32 v4, 0x4b400000, v4
	v_med3_f32 v5, v5, s29, v222
	v_med3_f32 v6, v6, s29, v222
	v_add_f32_e32 v3, 0x4b400000, v3
	v_add_f32_e32 v5, 0x4b400000, v5
	v_add_f32_e32 v6, 0x4b400000, v6
	s_movk_i32 s8, 0x7f
	s_movk_i32 s9, 0xff81
	s_nop 0
	v_lshlrev_b32_e32 v5, 16, v5
	v_lshlrev_b32_e32 v4, 8, v4
	v_and_b32_e32 v4, 0xff00, v4
	v_and_b32_e32 v5, 0xff0000, v5
	v_perm_b32 v3, v6, v3, s24
	v_or3_b32 v3, v3, v4, v5
	global_store_dwordx4 v[70:71], v[0:3], off offset:64
	s_waitcnt lgkmcnt(0)
	s_barrier
	s_cbranch_scc0 .LBB0_132
